# attention: one static s_setprio 1 for waves 4-7 during the attention unit loop (reset after), on top of v034
# speedup vs baseline: 1.0024x; 1.0024x over previous
.LBB0_260:
	s_lshr_b32 s84, s21, 1
	s_bitcmp0_b32 s21, 0
	s_cselect_b32 s82, s49, s48
	s_lshl_b32 s0, s84, 7
	s_add_u32 s3, s52, s0
	s_addc_u32 s33, s53, 0
	s_add_u32 s39, s54, s0
	v_mov_b32_e32 v36, v0
	s_mov_b32 s38, s82
	s_mov_b32 s0, s4
	s_addc_u32 s43, s55, 0
	s_ashr_i32 s1, s0, 31
	v_readfirstlane_b32 s2, v36
	s_lshl_b64 s[34:35], s[0:1], 14
	s_lshl_b32 s1, s38, 8
	s_ashr_i32 s83, s2, 6
	s_cmp_lt_u32 s83, 4
	s_cbranch_scc1 .Lprio_p0
	s_setprio 1
.Lprio_p0:
	s_ashr_i32 s36, s1, 31
	s_add_u32 s34, s34, s1
	s_addc_u32 s35, s35, s36
	s_lshl_b32 s46, s83, 5
	s_ashr_i32 s36, s46, 31
	s_add_u32 s34, s34, s46
	s_addc_u32 s35, s35, s36
	s_mul_i32 s36, s35, 0x1200
	s_mul_hi_u32 s37, s34, 0x1200
	s_add_i32 s37, s37, s36
	s_mul_i32 s36, s34, 0x1200
	s_add_u32 s36, s3, s36
	s_addc_u32 s37, s33, s37
	s_mul_hi_i32 s3, s0, 0x4800000
	s_mul_i32 s0, s0, 0x4800000
	v_and_b32_e32 v230, 63, v36
	s_add_u32 s42, s39, s0
	s_addc_u32 s43, s43, s3
	v_mul_u32_u24_e32 v2, 0x900, v230
	s_add_u32 s44, s62, s0
	v_lshlrev_b32_e32 v2, 1, v2
	s_addc_u32 s45, s63, s3
	v_lshl_add_u64 v[4:5], s[42:43], 0, v[2:3]
	s_lshl_b32 s42, s83, 3
	s_lshl_b32 s0, s83, 4
	v_bfe_u32 v2, v36, 2, 4
	s_ashr_i32 s43, s42, 31
	v_and_or_b32 v2, s0, 48, v2
	s_ashr_i32 s0, s2, 3
	v_lshl_add_u64 v[216:217], s[42:43], 1, v[4:5]
	s_and_b32 s42, s0, 0xffffffe0
	v_mul_u32_u24_e32 v2, 0x900, v2
	s_ashr_i32 s43, s42, 31
	s_lshl_b32 s0, s83, 10
	v_lshlrev_b32_e32 v2, 1, v2
	v_lshlrev_b32_e32 v232, 3, v36
	s_cmp_lg_u32 0, -1
	v_lshl_add_u64 v[4:5], s[44:45], 0, v[2:3]
	v_and_b32_e32 v233, 24, v232
	s_cselect_b32 s3, 0, 0
	v_and_b32_e32 v231, 31, v36
	v_lshl_add_u64 v[4:5], s[42:43], 1, v[4:5]
	v_lshlrev_b32_e32 v2, 1, v233
	s_add_i32 s76, s0, s3
	s_mov_b32 m0, s76
	s_nop 0
	global_load_lds_dwordx4 v[216:217], off
	v_lshl_add_u64 v[218:219], v[4:5], 0, v[2:3]
	s_add_i32 s77, s76, 0x6000
	s_mov_b32 m0, s77
	s_nop 0
	global_load_lds_dwordx4 v[218:219], off
	s_mov_b64 s[42:43], 0x80
	v_mul_u32_u24_e32 v2, 0x900, v231
	v_bfe_u32 v229, v36, 5, 1
	v_lshl_add_u64 v[220:221], v[218:219], 0, s[42:43]
	s_add_i32 s3, s76, 0x8000
	s_mov_b32 m0, s3
	s_nop 0
	global_load_lds_dwordx4 v[220:221], off
	v_lshlrev_b32_e32 v2, 1, v2
	v_lshl_add_u64 v[4:5], v[216:217], 0, s[26:27]
	s_add_i32 s3, s76, 0x2000
	s_mov_b32 m0, s3
	s_nop 0
	global_load_lds_dwordx4 v[4:5], off
	v_lshl_or_b32 v2, v229, 4, v2
	global_load_dwordx4 v[154:157], v2, s[36:37]
	global_load_dwordx4 v[150:153], v2, s[36:37] offset:32
	global_load_dwordx4 v[146:149], v2, s[36:37] offset:64
	global_load_dwordx4 v[142:145], v2, s[36:37] offset:96
	s_mov_b64 s[36:37], 0x48080
	v_lshlrev_b32_e32 v2, 10, v229
	v_lshlrev_b32_e32 v4, 4, v231
	v_add3_u32 v240, 0, v2, v4
	v_lshl_add_u64 v[4:5], v[216:217], 0, s[28:29]
	s_add_i32 s3, s76, 0x4000
	v_lshl_add_u64 v[8:9], v[218:219], 0, s[36:37]
	s_mov_b32 m0, s3
	s_nop 0
	global_load_lds_dwordx4 v[4:5], off
	s_add_i32 s33, s76, 0xa000
	v_lshl_add_u64 v[6:7], v[218:219], 0, s[26:27]
	s_mov_b32 m0, s33
	s_nop 0
	global_load_lds_dwordx4 v[6:7], off
	s_add_i32 s39, s76, 0xc000
	s_mov_b32 m0, s39
	s_nop 0
	global_load_lds_dwordx4 v[8:9], off
	s_waitcnt vmcnt(6) lgkmcnt(0)
	s_barrier
	ds_read_b128 v[4:7], v240
	ds_read_b128 v[8:11], v240 offset:512
	ds_read_b128 v[38:41], v240 offset:2048
	ds_read_b128 v[42:45], v240 offset:2560
	s_add_i32 s3, s1, 0x100
	s_ashr_i32 s85, s3, 6
	v_lshlrev_b32_e32 v239, 2, v229
	v_or_b32_e32 v238, s46, v231
	s_cmp_gt_i32 s85, 4
	s_waitcnt vmcnt(3) lgkmcnt(3)
	v_mfma_f32_32x32x16_bf16 v[20:35], v[4:7], v[154:157], 0
	s_waitcnt lgkmcnt(2)
	v_mfma_f32_32x32x16_bf16 v[4:19], v[8:11], v[154:157], 0
	s_waitcnt vmcnt(2) lgkmcnt(1)
	v_mfma_f32_32x32x16_bf16 v[20:35], v[38:41], v[150:153], v[20:35]
	s_waitcnt lgkmcnt(0)
	v_mfma_f32_32x32x16_bf16 v[4:19], v[42:45], v[150:153], v[4:19]
	ds_read_b128 v[38:41], v240 offset:4096
	ds_read_b128 v[42:45], v240 offset:4608
	s_waitcnt vmcnt(1) lgkmcnt(1)
	v_mfma_f32_32x32x16_bf16 v[20:35], v[38:41], v[146:149], v[20:35]
	s_waitcnt lgkmcnt(0)
	v_mfma_f32_32x32x16_bf16 v[4:19], v[42:45], v[146:149], v[4:19]
	ds_read_b128 v[38:41], v240 offset:6144
	ds_read_b128 v[42:45], v240 offset:6656
	s_waitcnt vmcnt(0) lgkmcnt(1)
	v_mfma_f32_32x32x16_bf16 v[20:35], v[38:41], v[142:145], v[20:35]
	s_waitcnt lgkmcnt(0)
	v_mfma_f32_32x32x16_bf16 v[4:19], v[42:45], v[142:145], v[4:19]
	s_nop 15
	s_nop 7
	s_cbranch_scc1 .LBB0_262
	v_subrev_u32_e32 v2, s1, v239
	v_or_b32_e32 v37, 32, v2
	v_cmp_le_i32_e32 vcc, v37, v238
	v_or_b32_e32 v37, 33, v2
	s_nop 6
	v_cndmask_b32_e32 v4, v227, v4, vcc
	v_cmp_lt_i32_e32 vcc, v2, v238
	s_nop 1
	v_cndmask_b32_e32 v21, v227, v21, vcc
	v_cmp_le_i32_e32 vcc, v2, v238
	s_nop 1
	v_cndmask_b32_e32 v20, v227, v20, vcc
	v_cmp_le_i32_e32 vcc, v37, v238
	v_or_b32_e32 v37, 2, v2
	s_nop 0
	v_cndmask_b32_e32 v5, v227, v5, vcc
	v_cmp_le_i32_e32 vcc, v37, v238
	v_or_b32_e32 v37, 34, v2
	s_nop 0
	v_cndmask_b32_e32 v22, v227, v22, vcc
	v_cmp_le_i32_e32 vcc, v37, v238
	v_or_b32_e32 v37, 3, v2
	s_nop 0
	v_cndmask_b32_e32 v6, v227, v6, vcc
	v_cmp_le_i32_e32 vcc, v37, v238
	v_or_b32_e32 v37, 35, v2
	s_nop 0
	v_cndmask_b32_e32 v23, v227, v23, vcc
	v_cmp_le_i32_e32 vcc, v37, v238
	v_or_b32_e32 v37, 8, v2
	s_nop 0
	v_cndmask_b32_e32 v7, v227, v7, vcc
	v_cmp_le_i32_e32 vcc, v37, v238
	v_or_b32_e32 v37, 40, v2
	s_nop 0
	v_cndmask_b32_e32 v24, v227, v24, vcc
	v_cmp_le_i32_e32 vcc, v37, v238
	v_or_b32_e32 v37, 9, v2
	s_nop 0
	v_cndmask_b32_e32 v8, v227, v8, vcc
	v_cmp_le_i32_e32 vcc, v37, v238
	v_or_b32_e32 v37, 41, v2
	s_nop 0
	v_cndmask_b32_e32 v25, v227, v25, vcc
	v_cmp_le_i32_e32 vcc, v37, v238
	v_or_b32_e32 v37, 10, v2
	s_nop 0
	v_cndmask_b32_e32 v9, v227, v9, vcc
	v_cmp_le_i32_e32 vcc, v37, v238
	v_or_b32_e32 v37, 42, v2
	s_nop 0
	v_cndmask_b32_e32 v26, v227, v26, vcc
	v_cmp_le_i32_e32 vcc, v37, v238
	v_or_b32_e32 v37, 11, v2
	s_nop 0
	v_cndmask_b32_e32 v10, v227, v10, vcc
	v_cmp_le_i32_e32 vcc, v37, v238
	v_or_b32_e32 v37, 43, v2
	s_nop 0
	v_cndmask_b32_e32 v27, v227, v27, vcc
	v_cmp_le_i32_e32 vcc, v37, v238
	v_or_b32_e32 v37, 16, v2
	s_nop 0
	v_cndmask_b32_e32 v11, v227, v11, vcc
	v_cmp_le_i32_e32 vcc, v37, v238
	v_or_b32_e32 v37, 48, v2
	s_nop 0
	v_cndmask_b32_e32 v28, v227, v28, vcc
	v_cmp_le_i32_e32 vcc, v37, v238
	v_or_b32_e32 v37, 17, v2
	s_nop 0
	v_cndmask_b32_e32 v12, v227, v12, vcc
	v_cmp_le_i32_e32 vcc, v37, v238
	v_or_b32_e32 v37, 49, v2
	s_nop 0
	v_cndmask_b32_e32 v29, v227, v29, vcc
	v_cmp_le_i32_e32 vcc, v37, v238
	v_or_b32_e32 v37, 18, v2
	s_nop 0
	v_cndmask_b32_e32 v13, v227, v13, vcc
	v_cmp_le_i32_e32 vcc, v37, v238
	v_or_b32_e32 v37, 50, v2
	s_nop 0
	v_cndmask_b32_e32 v30, v227, v30, vcc
	v_cmp_le_i32_e32 vcc, v37, v238
	v_or_b32_e32 v37, 19, v2
	s_nop 0
	v_cndmask_b32_e32 v14, v227, v14, vcc
	v_cmp_le_i32_e32 vcc, v37, v238
	v_or_b32_e32 v37, 51, v2
	s_nop 0
	v_cndmask_b32_e32 v31, v227, v31, vcc
	v_cmp_le_i32_e32 vcc, v37, v238
	v_or_b32_e32 v37, 24, v2
	s_nop 0
	v_cndmask_b32_e32 v15, v227, v15, vcc
	v_cmp_le_i32_e32 vcc, v37, v238
	v_or_b32_e32 v37, 56, v2
	s_nop 0
	v_cndmask_b32_e32 v32, v227, v32, vcc
	v_cmp_le_i32_e32 vcc, v37, v238
	v_or_b32_e32 v37, 25, v2
	s_nop 0
	v_cndmask_b32_e32 v16, v227, v16, vcc
	v_cmp_le_i32_e32 vcc, v37, v238
	v_or_b32_e32 v37, 57, v2
	s_nop 0
	v_cndmask_b32_e32 v33, v227, v33, vcc
	v_cmp_le_i32_e32 vcc, v37, v238
	v_or_b32_e32 v37, 26, v2
	s_nop 0
	v_cndmask_b32_e32 v17, v227, v17, vcc
	v_cmp_le_i32_e32 vcc, v37, v238
	v_or_b32_e32 v37, 58, v2
	s_nop 0
	v_cndmask_b32_e32 v34, v227, v34, vcc
	v_cmp_le_i32_e32 vcc, v37, v238
	v_or_b32_e32 v37, 27, v2
	v_or_b32_e32 v2, 59, v2
	v_cndmask_b32_e32 v18, v227, v18, vcc
	v_cmp_le_i32_e32 vcc, v37, v238
	s_nop 1
	v_cndmask_b32_e32 v35, v227, v35, vcc
	v_cmp_le_i32_e32 vcc, v2, v238
	s_nop 1
	v_cndmask_b32_e32 v19, v227, v19, vcc

.LBB0_349:
	s_setprio 0
	v_mov_b32_e32 v52, v0
	s_barrier
	s_ashr_i32 s21, s20, 31
	v_readfirstlane_b32 s0, v52
	s_ashr_i32 s2, s0, 2
	s_and_b32 s36, s2, -16
	s_ashr_i32 s3, s0, 7
	v_lshlrev_b32_e32 v2, 4, v52
	v_and_b32_e32 v38, 48, v52
	v_mov_b32_e32 v39, 0
	v_and_b32_e32 v59, 48, v2
	v_lshl_add_u64 v[2:3], s[22:23], 0, v[38:39]
	s_mov_b64 s[0:1], 0x100000
	s_cmp_gt_i32 s3, -1
	v_lshl_add_u64 v[42:43], v[2:3], 0, s[0:1]
	s_cselect_b64 s[0:1], -1, 0
	s_cmp_gt_i32 s3, 0
	v_ashrrev_i32_e32 v58, 2, v52
	s_cselect_b64 s[24:25], -1, 0
	s_cmp_gt_i32 s3, 1
	s_movk_i32 s4, 0x1200
	v_and_b32_e32 v1, 63, v52
	s_cselect_b64 s[26:27], -1, 0
	s_cmp_gt_i32 s3, 2
	v_bfi_b32 v44, -16, s2, v52
	v_mad_i64_i32 v[2:3], s[2:3], v58, s4, 0
	v_mov_b32_e32 v8, 0x90000
	v_lshlrev_b32_e32 v1, 2, v1
	v_mad_i64_i32 v[2:3], s[2:3], s20, v8, v[2:3]
	v_xor_b32_e32 v45, 4, v1
	v_xor_b32_e32 v53, 8, v1
	s_cselect_b64 s[28:29], -1, 0
	v_and_b32_e32 v1, 3, v52
	s_add_u32 s2, s94, s41
	v_lshl_or_b32 v2, v1, 5, v2
	s_addc_u32 s3, s95, 0
	v_bfe_u32 v41, v52, 4, 2
	v_lshl_add_u64 v[46:47], s[2:3], 0, v[2:3]
	v_mad_i64_i32 v[2:3], s[4:5], v44, s4, 0
	v_lshlrev_b32_e32 v40, 3, v41
	v_mad_i64_i32 v[2:3], s[4:5], s20, v8, v[2:3]
	v_or_b32_e32 v2, v2, v40
	v_and_b32_e32 v55, 15, v52
	v_lshl_add_u64 v[2:3], s[2:3], 0, v[2:3]
	s_mov_b64 s[2:3], 0x10a00040
	v_lshl_add_u32 v4, v58, 1, 0
	v_add_u32_e32 v5, 0, v38
	v_mul_u32_u24_e32 v6, 0x110, v59
	v_mul_u32_u24_e32 v7, 0x110, v55
	v_lshl_add_u64 v[48:49], v[2:3], 0, s[2:3]
	v_cndmask_b32_e64 v2, 0, 1, s[0:1]
	s_mov_b64 s[30:31], 0
	s_mov_b64 s[34:35], 0x10a00200
	v_mov_b32_e32 v39, 0x3727c5ac
	s_mov_b32 s33, 0xf800000
	v_mov_b32_e32 v54, 0x260
	s_movk_i32 s37, 0x7fff
	v_add_u32_e32 v56, v4, v6
	v_cmp_ne_u32_e64 s[2:3], 1, v2
	v_add_u32_e32 v57, v5, v7
	v_mov_b32_e32 v60, 1
	v_readlane_b32 s41, v254, 39
	s_branch .LBB0_351

.LBB0_873:
	s_lshr_b32 s42, s21, 1
	s_bitcmp0_b32 s21, 0
	s_cselect_b32 s63, s50, s47
	s_lshl_b32 s0, s42, 7
	s_add_u32 s3, s51, s0
	s_addc_u32 s29, s52, 0
	s_add_u32 s31, s53, s0
	v_mov_b32_e32 v36, v0
	s_mov_b32 s30, s63
	s_mov_b32 s0, s4
	s_addc_u32 s35, s55, 0
	s_ashr_i32 s1, s0, 31
	v_readfirstlane_b32 s2, v36
	s_lshl_b64 s[26:27], s[0:1], 14
	s_lshl_b32 s1, s30, 8
	s_ashr_i32 s33, s2, 6
	s_cmp_lt_u32 s33, 4
	s_cbranch_scc1 .Lprio_p1
	s_setprio 1
.Lprio_p1:
	s_ashr_i32 s28, s1, 31
	s_add_u32 s26, s26, s1
	s_addc_u32 s27, s27, s28
	s_lshl_b32 s38, s33, 5
	s_ashr_i32 s28, s38, 31
	s_add_u32 s26, s26, s38
	s_addc_u32 s27, s27, s28
	s_mul_i32 s28, s27, 0x1200
	s_mul_hi_u32 s34, s26, 0x1200
	s_add_i32 s34, s34, s28
	s_mul_i32 s28, s26, 0x1200
	s_add_u32 s28, s3, s28
	s_addc_u32 s29, s29, s34
	s_mul_hi_i32 s3, s0, 0x4800000
	s_mul_i32 s0, s0, 0x4800000
	v_and_b32_e32 v230, 63, v36
	s_add_u32 s34, s31, s0
	s_addc_u32 s35, s35, s3
	v_mul_u32_u24_e32 v2, 0x900, v230
	s_add_u32 s36, s56, s0
	v_lshlrev_b32_e32 v2, 1, v2
	s_addc_u32 s37, s57, s3
	v_lshl_add_u64 v[4:5], s[34:35], 0, v[2:3]
	s_lshl_b32 s34, s33, 3
	s_lshl_b32 s0, s33, 4
	v_bfe_u32 v2, v36, 2, 4
	s_ashr_i32 s35, s34, 31
	v_and_or_b32 v2, s0, 48, v2
	s_ashr_i32 s0, s2, 3
	v_lshl_add_u64 v[216:217], s[34:35], 1, v[4:5]
	s_and_b32 s34, s0, 0xffffffe0
	v_mul_u32_u24_e32 v2, 0x900, v2
	s_ashr_i32 s35, s34, 31
	s_lshl_b32 s0, s33, 10
	v_lshlrev_b32_e32 v2, 1, v2
	v_lshlrev_b32_e32 v232, 3, v36
	s_cmp_lg_u32 0, -1
	v_lshl_add_u64 v[4:5], s[36:37], 0, v[2:3]
	v_and_b32_e32 v233, 24, v232
	s_cselect_b32 s3, 0, 0
	v_and_b32_e32 v231, 31, v36
	v_lshl_add_u64 v[4:5], s[34:35], 1, v[4:5]
	v_lshlrev_b32_e32 v2, 1, v233
	s_add_i32 s76, s0, s3
	s_mov_b32 m0, s76
	s_nop 0
	global_load_lds_dwordx4 v[216:217], off
	v_lshl_add_u64 v[218:219], v[4:5], 0, v[2:3]
	s_add_i32 s77, s76, 0x6000
	s_mov_b32 m0, s77
	s_nop 0
	global_load_lds_dwordx4 v[218:219], off
	s_mov_b64 s[34:35], 0x80
	v_mul_u32_u24_e32 v2, 0x900, v231
	v_bfe_u32 v229, v36, 5, 1
	v_lshl_add_u64 v[220:221], v[218:219], 0, s[34:35]
	s_add_i32 s3, s76, 0x8000
	s_mov_b32 m0, s3
	s_nop 0
	global_load_lds_dwordx4 v[220:221], off
	v_lshlrev_b32_e32 v2, 1, v2
	v_lshl_add_u64 v[4:5], v[216:217], 0, s[18:19]
	s_add_i32 s3, s76, 0x2000
	s_mov_b32 m0, s3
	s_nop 0
	global_load_lds_dwordx4 v[4:5], off
	v_lshl_or_b32 v2, v229, 4, v2
	global_load_dwordx4 v[154:157], v2, s[28:29]
	global_load_dwordx4 v[150:153], v2, s[28:29] offset:32
	global_load_dwordx4 v[146:149], v2, s[28:29] offset:64
	global_load_dwordx4 v[142:145], v2, s[28:29] offset:96
	s_mov_b64 s[28:29], 0x48080
	v_lshlrev_b32_e32 v2, 10, v229
	v_lshlrev_b32_e32 v4, 4, v231
	v_add3_u32 v240, 0, v2, v4
	v_lshl_add_u64 v[4:5], v[216:217], 0, s[22:23]
	s_add_i32 s3, s76, 0x4000
	v_lshl_add_u64 v[8:9], v[218:219], 0, s[28:29]
	s_mov_b32 m0, s3
	s_nop 0
	global_load_lds_dwordx4 v[4:5], off
	s_add_i32 s31, s76, 0xa000
	v_lshl_add_u64 v[6:7], v[218:219], 0, s[18:19]
	s_mov_b32 m0, s31
	s_nop 0
	global_load_lds_dwordx4 v[6:7], off
	s_add_i32 s34, s76, 0xc000
	s_mov_b32 m0, s34
	s_nop 0
	global_load_lds_dwordx4 v[8:9], off
	s_waitcnt vmcnt(6) lgkmcnt(0)
	s_barrier
	ds_read_b128 v[4:7], v240
	ds_read_b128 v[8:11], v240 offset:512
	ds_read_b128 v[38:41], v240 offset:2048
	ds_read_b128 v[42:45], v240 offset:2560
	s_add_i32 s3, s1, 0x100
	s_ashr_i32 s79, s3, 6
	v_lshlrev_b32_e32 v239, 2, v229
	v_or_b32_e32 v238, s38, v231
	s_cmp_gt_i32 s79, 4
	s_waitcnt vmcnt(3) lgkmcnt(3)
	v_mfma_f32_32x32x16_bf16 v[20:35], v[4:7], v[154:157], 0
	s_waitcnt lgkmcnt(2)
	v_mfma_f32_32x32x16_bf16 v[4:19], v[8:11], v[154:157], 0
	s_waitcnt vmcnt(2) lgkmcnt(1)
	v_mfma_f32_32x32x16_bf16 v[20:35], v[38:41], v[150:153], v[20:35]
	s_waitcnt lgkmcnt(0)
	v_mfma_f32_32x32x16_bf16 v[4:19], v[42:45], v[150:153], v[4:19]
	ds_read_b128 v[38:41], v240 offset:4096
	ds_read_b128 v[42:45], v240 offset:4608
	s_waitcnt vmcnt(1) lgkmcnt(1)
	v_mfma_f32_32x32x16_bf16 v[20:35], v[38:41], v[146:149], v[20:35]
	s_waitcnt lgkmcnt(0)
	v_mfma_f32_32x32x16_bf16 v[4:19], v[42:45], v[146:149], v[4:19]
	ds_read_b128 v[38:41], v240 offset:6144
	ds_read_b128 v[42:45], v240 offset:6656
	s_waitcnt vmcnt(0) lgkmcnt(1)
	v_mfma_f32_32x32x16_bf16 v[20:35], v[38:41], v[142:145], v[20:35]
	s_waitcnt lgkmcnt(0)
	v_mfma_f32_32x32x16_bf16 v[4:19], v[42:45], v[142:145], v[4:19]
	s_nop 15
	s_nop 7
	s_cbranch_scc1 .LBB0_875
	v_subrev_u32_e32 v2, s1, v239
	v_or_b32_e32 v37, 32, v2
	v_cmp_le_i32_e32 vcc, v37, v238
	v_or_b32_e32 v37, 33, v2
	s_nop 6
	v_cndmask_b32_e32 v4, v227, v4, vcc
	v_cmp_lt_i32_e32 vcc, v2, v238
	s_nop 1
	v_cndmask_b32_e32 v21, v227, v21, vcc
	v_cmp_le_i32_e32 vcc, v2, v238
	s_nop 1
	v_cndmask_b32_e32 v20, v227, v20, vcc
	v_cmp_le_i32_e32 vcc, v37, v238
	v_or_b32_e32 v37, 2, v2
	s_nop 0
	v_cndmask_b32_e32 v5, v227, v5, vcc
	v_cmp_le_i32_e32 vcc, v37, v238
	v_or_b32_e32 v37, 34, v2
	s_nop 0
	v_cndmask_b32_e32 v22, v227, v22, vcc
	v_cmp_le_i32_e32 vcc, v37, v238
	v_or_b32_e32 v37, 3, v2
	s_nop 0
	v_cndmask_b32_e32 v6, v227, v6, vcc
	v_cmp_le_i32_e32 vcc, v37, v238
	v_or_b32_e32 v37, 35, v2
	s_nop 0
	v_cndmask_b32_e32 v23, v227, v23, vcc
	v_cmp_le_i32_e32 vcc, v37, v238
	v_or_b32_e32 v37, 8, v2
	s_nop 0
	v_cndmask_b32_e32 v7, v227, v7, vcc
	v_cmp_le_i32_e32 vcc, v37, v238
	v_or_b32_e32 v37, 40, v2
	s_nop 0
	v_cndmask_b32_e32 v24, v227, v24, vcc
	v_cmp_le_i32_e32 vcc, v37, v238
	v_or_b32_e32 v37, 9, v2
	s_nop 0
	v_cndmask_b32_e32 v8, v227, v8, vcc
	v_cmp_le_i32_e32 vcc, v37, v238
	v_or_b32_e32 v37, 41, v2
	s_nop 0
	v_cndmask_b32_e32 v25, v227, v25, vcc
	v_cmp_le_i32_e32 vcc, v37, v238
	v_or_b32_e32 v37, 10, v2
	s_nop 0
	v_cndmask_b32_e32 v9, v227, v9, vcc
	v_cmp_le_i32_e32 vcc, v37, v238
	v_or_b32_e32 v37, 42, v2
	s_nop 0
	v_cndmask_b32_e32 v26, v227, v26, vcc
	v_cmp_le_i32_e32 vcc, v37, v238
	v_or_b32_e32 v37, 11, v2
	s_nop 0
	v_cndmask_b32_e32 v10, v227, v10, vcc
	v_cmp_le_i32_e32 vcc, v37, v238
	v_or_b32_e32 v37, 43, v2
	s_nop 0
	v_cndmask_b32_e32 v27, v227, v27, vcc
	v_cmp_le_i32_e32 vcc, v37, v238
	v_or_b32_e32 v37, 16, v2
	s_nop 0
	v_cndmask_b32_e32 v11, v227, v11, vcc
	v_cmp_le_i32_e32 vcc, v37, v238
	v_or_b32_e32 v37, 48, v2
	s_nop 0
	v_cndmask_b32_e32 v28, v227, v28, vcc
	v_cmp_le_i32_e32 vcc, v37, v238
	v_or_b32_e32 v37, 17, v2
	s_nop 0
	v_cndmask_b32_e32 v12, v227, v12, vcc
	v_cmp_le_i32_e32 vcc, v37, v238
	v_or_b32_e32 v37, 49, v2
	s_nop 0
	v_cndmask_b32_e32 v29, v227, v29, vcc
	v_cmp_le_i32_e32 vcc, v37, v238
	v_or_b32_e32 v37, 18, v2
	s_nop 0
	v_cndmask_b32_e32 v13, v227, v13, vcc
	v_cmp_le_i32_e32 vcc, v37, v238
	v_or_b32_e32 v37, 50, v2
	s_nop 0
	v_cndmask_b32_e32 v30, v227, v30, vcc
	v_cmp_le_i32_e32 vcc, v37, v238
	v_or_b32_e32 v37, 19, v2
	s_nop 0
	v_cndmask_b32_e32 v14, v227, v14, vcc
	v_cmp_le_i32_e32 vcc, v37, v238
	v_or_b32_e32 v37, 51, v2
	s_nop 0
	v_cndmask_b32_e32 v31, v227, v31, vcc
	v_cmp_le_i32_e32 vcc, v37, v238
	v_or_b32_e32 v37, 24, v2
	s_nop 0
	v_cndmask_b32_e32 v15, v227, v15, vcc
	v_cmp_le_i32_e32 vcc, v37, v238
	v_or_b32_e32 v37, 56, v2
	s_nop 0
	v_cndmask_b32_e32 v32, v227, v32, vcc
	v_cmp_le_i32_e32 vcc, v37, v238
	v_or_b32_e32 v37, 25, v2
	s_nop 0
	v_cndmask_b32_e32 v16, v227, v16, vcc
	v_cmp_le_i32_e32 vcc, v37, v238
	v_or_b32_e32 v37, 57, v2
	s_nop 0
	v_cndmask_b32_e32 v33, v227, v33, vcc
	v_cmp_le_i32_e32 vcc, v37, v238
	v_or_b32_e32 v37, 26, v2
	s_nop 0
	v_cndmask_b32_e32 v17, v227, v17, vcc
	v_cmp_le_i32_e32 vcc, v37, v238
	v_or_b32_e32 v37, 58, v2
	s_nop 0
	v_cndmask_b32_e32 v34, v227, v34, vcc
	v_cmp_le_i32_e32 vcc, v37, v238
	v_or_b32_e32 v37, 27, v2
	v_or_b32_e32 v2, 59, v2
	v_cndmask_b32_e32 v18, v227, v18, vcc
	v_cmp_le_i32_e32 vcc, v37, v238
	s_nop 1
	v_cndmask_b32_e32 v35, v227, v35, vcc
	v_cmp_le_i32_e32 vcc, v2, v238
	s_nop 1
	v_cndmask_b32_e32 v19, v227, v19, vcc

.LBB0_962:
	s_setprio 0
	v_mov_b32_e32 v52, v0
	s_barrier
	s_ashr_i32 s21, s20, 31
	v_readfirstlane_b32 s0, v52
	s_ashr_i32 s2, s0, 2
	s_and_b32 s29, s2, -16
	s_ashr_i32 s3, s0, 7
	v_lshlrev_b32_e32 v2, 4, v52
	v_and_b32_e32 v38, 48, v52
	v_mov_b32_e32 v39, 0
	v_and_b32_e32 v59, 48, v2
	v_lshl_add_u64 v[2:3], s[14:15], 0, v[38:39]
	s_mov_b64 s[0:1], 0x120000
	s_cmp_gt_i32 s3, -1
	v_lshl_add_u64 v[42:43], v[2:3], 0, s[0:1]
	s_cselect_b64 s[0:1], -1, 0
	s_cmp_gt_i32 s3, 0
	v_ashrrev_i32_e32 v58, 2, v52
	s_cselect_b64 s[16:17], -1, 0
	s_cmp_gt_i32 s3, 1
	s_movk_i32 s4, 0x1200
	v_and_b32_e32 v1, 63, v52
	s_cselect_b64 s[18:19], -1, 0
	s_cmp_gt_i32 s3, 2
	v_bfi_b32 v44, -16, s2, v52
	v_mad_i64_i32 v[2:3], s[2:3], v58, s4, 0
	v_mov_b32_e32 v8, 0x90000
	v_lshlrev_b32_e32 v1, 2, v1
	v_mad_i64_i32 v[2:3], s[2:3], s20, v8, v[2:3]
	v_xor_b32_e32 v45, 4, v1
	v_xor_b32_e32 v53, 8, v1
	s_cselect_b64 s[22:23], -1, 0
	v_and_b32_e32 v1, 3, v52
	s_add_u32 s2, s94, s46
	v_lshl_or_b32 v2, v1, 5, v2
	s_addc_u32 s3, s95, 0
	v_bfe_u32 v41, v52, 4, 2
	v_lshl_add_u64 v[46:47], s[2:3], 0, v[2:3]
	v_mad_i64_i32 v[2:3], s[4:5], v44, s4, 0
	v_lshlrev_b32_e32 v40, 3, v41
	v_mad_i64_i32 v[2:3], s[4:5], s20, v8, v[2:3]
	v_or_b32_e32 v2, v2, v40
	v_and_b32_e32 v55, 15, v52
	v_lshl_add_u64 v[2:3], s[2:3], 0, v[2:3]
	s_mov_b64 s[2:3], 0x10a00040
	v_lshl_add_u32 v4, v58, 1, 0
	v_add_u32_e32 v5, 0, v38
	v_mul_u32_u24_e32 v6, 0x110, v59
	v_mul_u32_u24_e32 v7, 0x110, v55
	v_lshl_add_u64 v[48:49], v[2:3], 0, s[2:3]
	v_cndmask_b32_e64 v2, 0, 1, s[0:1]
	s_mov_b64 s[24:25], 0
	s_mov_b64 s[26:27], 0x10a00200
	v_mov_b32_e32 v39, 0x3727c5ac
	s_mov_b32 s28, 0xf800000
	v_mov_b32_e32 v54, 0x260
	s_movk_i32 s30, 0x7fff
	v_add_u32_e32 v56, v4, v6
	v_cmp_ne_u32_e64 s[2:3], 1, v2
	v_add_u32_e32 v57, v5, v7
	v_mov_b32_e32 v60, 1
	v_readlane_b32 s51, v254, 39
	s_branch .LBB0_964
